# adds non-temporal stores for bf16 MoE weight conversion in the mix phase on top of v33
# speedup vs baseline: 1.0107x; 1.0107x over previous
.LBB0_1126:
	ds_write2_b32 v86, v34, v35 offset1:1
	ds_write2_b32 v86, v36, v37 offset0:2 offset1:3
	ds_write2_b32 v87, v38, v39 offset1:1
	ds_write2_b32 v88, v40, v41 offset1:1
	ds_write2_b32 v89, v42, v43 offset1:1
	ds_write2_b32 v90, v44, v45 offset1:1
	ds_write2_b32 v91, v46, v47 offset1:1
	ds_write2_b32 v92, v48, v49 offset1:1
	ds_write2_b32 v93, v54, v55 offset1:1
	ds_write2_b32 v94, v56, v57 offset1:1
	ds_write2_b32 v95, v50, v51 offset1:1
	ds_write2_b32 v96, v52, v53 offset1:1
	ds_write2_b32 v97, v62, v63 offset1:1
	ds_write2_b32 v98, v64, v65 offset1:1
	ds_write2_b32 v99, v58, v59 offset1:1
	ds_write2_b32 v102, v60, v61 offset1:1
	s_waitcnt lgkmcnt(0)
	ds_read2_b32 v[94:95], v85 offset0:33 offset1:41
	ds_read2_b32 v[96:97], v85 offset1:8
	ds_read2_b32 v[98:99], v85 offset0:66 offset1:74
	ds_read2_b32 v[102:103], v85 offset0:99 offset1:107
	ds_read2_b32 v[104:105], v85 offset0:132 offset1:140
	ds_read2_b32 v[106:107], v85 offset0:165 offset1:173
	ds_read2_b32 v[108:109], v85 offset0:198 offset1:206
	ds_read2_b32 v[110:111], v85 offset0:231 offset1:239
	v_lshl_add_u64 v[92:93], s[8:9], 0, v[100:101]
	s_waitcnt lgkmcnt(6)
	v_cvt_pk_bf16_f32 v88, v96, v94
	s_waitcnt lgkmcnt(4)
	v_cvt_pk_bf16_f32 v89, v98, v102
	s_waitcnt lgkmcnt(2)
	v_cvt_pk_bf16_f32 v90, v104, v106
	s_waitcnt lgkmcnt(0)
	v_cvt_pk_bf16_f32 v91, v108, v110
	v_lshl_add_u64 v[112:113], v[92:93], 0, v[70:71]
	global_store_dwordx4 v[112:113], v[88:91], off nt
	v_lshl_add_u64 v[112:113], v[92:93], 0, v[74:75]
	s_add_i32 s36, s36, 16
	v_cvt_pk_bf16_f32 v88, v97, v95
	v_cvt_pk_bf16_f32 v89, v99, v103
	v_cvt_pk_bf16_f32 v90, v105, v107
	v_cvt_pk_bf16_f32 v91, v109, v111
	v_lshl_add_u64 v[94:95], v[92:93], 0, v[72:73]
	global_store_dwordx4 v[94:95], v[88:91], off nt
	ds_read2_b32 v[94:95], v85 offset0:49 offset1:57
	ds_read2_b32 v[96:97], v85 offset0:16 offset1:24
	ds_read2_b32 v[98:99], v85 offset0:82 offset1:90
	ds_read2_b32 v[102:103], v85 offset0:115 offset1:123
	ds_read2_b32 v[104:105], v85 offset0:148 offset1:156
	ds_read2_b32 v[106:107], v85 offset0:181 offset1:189
	ds_read2_b32 v[108:109], v85 offset0:214 offset1:222
	ds_read2_b32 v[110:111], v85 offset0:247 offset1:255
	v_lshl_add_u64 v[92:93], v[92:93], 0, v[76:77]
	s_waitcnt lgkmcnt(6)
	v_cvt_pk_bf16_f32 v88, v96, v94
	s_waitcnt lgkmcnt(4)
	v_cvt_pk_bf16_f32 v89, v98, v102
	s_waitcnt lgkmcnt(2)
	v_cvt_pk_bf16_f32 v90, v104, v106
	s_waitcnt lgkmcnt(0)
	v_cvt_pk_bf16_f32 v91, v108, v110
	global_store_dwordx4 v[112:113], v[88:91], off nt
	s_addk_i32 s37, 0x200
	s_add_i32 s38, s38, 32
	v_cvt_pk_bf16_f32 v88, v97, v95
	v_cvt_pk_bf16_f32 v89, v99, v103
	v_cvt_pk_bf16_f32 v90, v105, v107
	v_cvt_pk_bf16_f32 v91, v109, v111
	global_store_dwordx4 v[92:93], v[88:91], off nt
	s_waitcnt lgkmcnt(0)
	s_cmp_ge_i32 s24, s35
	s_cselect_b64 s[10:11], -1, 0

.LBB0_1138:
	v_add_u32_e32 v87, 0x420, v86
	v_add_u32_e32 v88, 0x428, v86
	v_add_u32_e32 v89, 0x840, v86
	v_add_u32_e32 v90, 0x848, v86
	v_add_u32_e32 v91, 0xc60, v86
	v_add_u32_e32 v92, 0xc68, v86
	v_add_u32_e32 v93, 0x1080, v86
	v_add_u32_e32 v94, 0x1088, v86
	v_add_u32_e32 v95, 0x14a0, v86
	v_add_u32_e32 v96, 0x14a8, v86
	v_add_u32_e32 v97, 0x18c0, v86
	v_add_u32_e32 v98, 0x18c8, v86
	v_add_u32_e32 v99, 0x1ce0, v86
	v_add_u32_e32 v102, 0x1ce8, v86
	s_waitcnt vmcnt(7)
	ds_write2_b32 v86, v2, v3 offset1:1
	ds_write2_b32 v86, v4, v5 offset0:2 offset1:3
	s_waitcnt vmcnt(6)
	ds_write2_b32 v87, v6, v7 offset1:1
	ds_write2_b32 v88, v8, v9 offset1:1
	s_waitcnt vmcnt(5)
	ds_write2_b32 v89, v10, v11 offset1:1
	ds_write2_b32 v90, v12, v13 offset1:1
	s_waitcnt vmcnt(4)
	ds_write2_b32 v91, v14, v15 offset1:1
	ds_write2_b32 v92, v16, v17 offset1:1
	s_waitcnt vmcnt(3)
	ds_write2_b32 v93, v18, v19 offset1:1
	ds_write2_b32 v94, v20, v21 offset1:1
	s_waitcnt vmcnt(2)
	ds_write2_b32 v95, v22, v23 offset1:1
	ds_write2_b32 v96, v24, v25 offset1:1
	s_waitcnt vmcnt(1)
	ds_write2_b32 v97, v26, v27 offset1:1
	ds_write2_b32 v98, v28, v29 offset1:1
	s_waitcnt vmcnt(0)
	ds_write2_b32 v99, v30, v31 offset1:1
	ds_write2_b32 v102, v32, v33 offset1:1
	s_waitcnt lgkmcnt(0)
	ds_read2_b32 v[108:109], v85 offset0:33 offset1:41
	ds_read2_b32 v[110:111], v85 offset1:8
	ds_read2_b32 v[112:113], v85 offset0:66 offset1:74
	ds_read2_b32 v[114:115], v85 offset0:99 offset1:107
	ds_read2_b32 v[116:117], v85 offset0:132 offset1:140
	ds_read2_b32 v[118:119], v85 offset0:165 offset1:173
	ds_read2_b32 v[120:121], v85 offset0:198 offset1:206
	ds_read2_b32 v[122:123], v85 offset0:231 offset1:239
	v_lshlrev_b32_e32 v100, 1, v68
	v_lshl_add_u64 v[124:125], s[6:7], 0, v[100:101]
	s_waitcnt lgkmcnt(6)
	v_cvt_pk_bf16_f32 v104, v110, v108
	s_waitcnt lgkmcnt(4)
	v_cvt_pk_bf16_f32 v105, v112, v114
	s_waitcnt lgkmcnt(2)
	v_cvt_pk_bf16_f32 v106, v116, v118
	s_waitcnt lgkmcnt(0)
	v_cvt_pk_bf16_f32 v107, v120, v122
	v_lshl_add_u64 v[126:127], v[124:125], 0, v[70:71]
	global_store_dwordx4 v[126:127], v[104:107], off nt
	s_andn2_b64 vcc, exec, s[10:11]
	s_mov_b64 s[10:11], -1
	v_cvt_pk_bf16_f32 v104, v111, v109
	v_cvt_pk_bf16_f32 v105, v113, v115
	v_cvt_pk_bf16_f32 v106, v117, v119
	v_cvt_pk_bf16_f32 v107, v121, v123
	ds_read2_b32 v[110:111], v85 offset0:49 offset1:57
	ds_read2_b32 v[112:113], v85 offset0:16 offset1:24
	ds_read2_b32 v[114:115], v85 offset0:82 offset1:90
	ds_read2_b32 v[116:117], v85 offset0:115 offset1:123
	ds_read2_b32 v[118:119], v85 offset0:148 offset1:156
	ds_read2_b32 v[120:121], v85 offset0:181 offset1:189
	ds_read2_b32 v[122:123], v85 offset0:214 offset1:222
	ds_read2_b32 v[126:127], v85 offset0:247 offset1:255
	v_lshl_add_u64 v[108:109], v[124:125], 0, v[72:73]
	global_store_dwordx4 v[108:109], v[104:107], off nt
	v_lshl_add_u64 v[108:109], v[124:125], 0, v[74:75]
	s_waitcnt lgkmcnt(6)
	v_cvt_pk_bf16_f32 v104, v112, v110
	s_waitcnt lgkmcnt(4)
	v_cvt_pk_bf16_f32 v105, v114, v116
	s_waitcnt lgkmcnt(2)
	v_cvt_pk_bf16_f32 v106, v118, v120
	s_waitcnt lgkmcnt(0)
	v_cvt_pk_bf16_f32 v107, v122, v126
	global_store_dwordx4 v[108:109], v[104:107], off nt
	v_lshl_add_u64 v[108:109], v[124:125], 0, v[76:77]
	s_nop 0
	v_cvt_pk_bf16_f32 v104, v113, v111
	v_cvt_pk_bf16_f32 v105, v115, v117
	v_cvt_pk_bf16_f32 v106, v119, v121
	v_cvt_pk_bf16_f32 v107, v123, v127
	global_store_dwordx4 v[108:109], v[104:107], off nt
	s_waitcnt lgkmcnt(0)
	s_cbranch_vccnz .LBB0_1127
	s_add_i32 s24, s36, 0x8008
	s_cmp_ge_i32 s24, s35
	s_cbranch_scc1 .LBB0_1126
	s_cmpk_gt_i32 s39, 0x7fef
	s_mov_b64 s[18:19], -1
	s_cbranch_scc0 .LBB0_1142
	v_readlane_b32 s6, v253, 23
	s_mov_b64 s[18:19], 0
	s_nop 0
	v_mov_b32_e32 v2, s6
	ds_read_b64 v[2:3], v2
	s_add_i32 s6, s36, 8
	s_lshr_b32 s6, s6, 9
	s_add_i32 s16, s6, s27
	s_lshl_b64 s[6:7], s[16:17], 22
	s_waitcnt lgkmcnt(0)
	v_readfirstlane_b32 s11, v2
	v_readfirstlane_b32 s10, v3
	s_add_u32 s12, s11, s6
	s_addc_u32 s13, s10, s7
	s_lshl_b64 s[6:7], s[16:17], 21
	s_add_u32 s10, s28, s6
	s_addc_u32 s11, s29, s7
	s_and_b32 s16, s38, 0x3c0
	s_and_b32 s6, s37, 0x3e0
	s_lshl_b32 s7, s16, 12
	s_add_u32 s12, s12, s7
	s_addc_u32 s13, s13, 0
	s_lshl_b32 s14, s6, 2
	s_add_u32 s14, s12, s14
	s_mov_b32 s7, s17
	s_addc_u32 s15, s13, 0
	s_mov_b64 s[12:13], s[16:17]
